# baseline (speedup 1.0000x reference)
.LBB0_17:
	s_andn2_b64 vcc, exec, s[4:5]
	s_cbranch_vccnz .LBB0_21
	s_load_dwordx8 s[4:11], s[0:1], 0x0
	s_load_dwordx4 s[12:15], s[0:1], 0x20
	s_load_dwordx4 s[16:19], s[0:1], 0x50
	s_sub_i32 s20, s2, 0x80
	s_cmpk_ge_i32 s20, 0x90
	s_cselect_b32 s21, 0x90, 0
	s_sub_i32 s20, s20, s21
	s_lshr_b32 s22, s20, 4
	s_and_b32 s23, s20, 15
	s_lshr_b32 s24, s23, 2
	s_and_b32 s25, s23, 3
	v_readfirstlane_b32 s26, v0
	s_nop 3
	s_lshr_b32 s26, s26, 6
	v_and_b32_e32 v1, 63, v0
	v_and_b32_e32 v2, 31, v1
	v_lshrrev_b32_e32 v3, 5, v1
	v_lshlrev_b32_e32 v4, 9, v2
	v_lshl_add_u32 v4, v3, 4, v4
	s_lshl_b32 s27, s22, 7
	s_lshl_b32 s29, s25, 5
	s_add_u32 s27, s27, s29
	s_lshl_b32 s27, s27, 9
	s_lshl_b32 s29, s26, 5
	s_add_u32 s27, s27, s29
	s_lshl_b32 s28, s24, 14
	s_add_u32 s28, s28, s29
	s_waitcnt lgkmcnt(0)
	s_cmp_lg_u32 s21, 0
	s_cselect_b32 s4, s8, s4
	s_cselect_b32 s5, s9, s5
	s_cselect_b32 s6, s10, s6
	s_cselect_b32 s7, s11, s7
	s_cselect_b32 s12, s14, s12
	s_cselect_b32 s13, s15, s13
	s_cselect_b32 s16, s18, s16
	s_cselect_b32 s17, s19, s17
	s_add_u32 s4, s4, s27
	s_addc_u32 s5, s5, 0
	s_add_u32 s6, s6, s27
	s_addc_u32 s7, s7, 0
	s_add_u32 s12, s12, s28
	s_addc_u32 s13, s13, 0
	global_load_dwordx4 v[8:11], v4, s[4:5]
	global_load_dwordx4 v[12:15], v4, s[6:7]
	global_load_dwordx4 v[40:43], v4, s[12:13]
	s_lshl_b32 s30, s24, 3
	s_add_u32 s30, s30, s25
	s_lshl_b32 s30, s30, 9
	s_lshr_b32 s31, s26, 2
	s_lshl_b32 s31, s31, 7
	s_add_u32 s30, s30, s31
	s_and_b32 s31, s26, 3
	s_add_u32 s30, s30, s31
	s_lshl_b32 s30, s30, 1
	s_lshl_b32 s31, s22, 15
	s_add_u32 s30, s30, s31
	s_add_u32 s16, s16, s30
	s_addc_u32 s17, s17, 0
	v_lshrrev_b32_e32 v6, 4, v2
	v_and_b32_e32 v7, 15, v2
	v_lshlrev_b32_e32 v6, 11, v6
	v_lshl_add_u32 v6, v7, 3, v6
	v_lshl_add_u32 v6, v3, 2, v6
	v_lshlrev_b32_e32 v6, 1, v6
	v_lshlrev_b32_e32 v5, 2, v1
	s_lshl_b32 s30, s26, 12
	v_add_u32_e32 v32, s30, v5
	s_lshl_b32 s30, s26, 8
	v_add_u32_e32 v33, s30, v5
	s_waitcnt vmcnt(1)
	v_pk_add_f32 v[8:9], v[8:9], v[12:13]
	v_pk_add_f32 v[10:11], v[10:11], v[14:15]
	s_waitcnt vmcnt(0)
	s_nop 1
	v_mfma_f32_32x32x2_f32 v[16:31], v8, v40, 0
	v_mfma_f32_32x32x2_f32 v[16:31], v9, v41, v[16:31]
	v_mfma_f32_32x32x2_f32 v[16:31], v10, v42, v[16:31]
	v_mfma_f32_32x32x2_f32 v[16:31], v11, v43, v[16:31]
	s_nop 15
	s_nop 3
	ds_write_b32 v32, v16 offset:0
	ds_write_b32 v32, v17 offset:256
	ds_write_b32 v32, v18 offset:512
	ds_write_b32 v32, v19 offset:768
	ds_write_b32 v32, v20 offset:1024
	ds_write_b32 v32, v21 offset:1280
	ds_write_b32 v32, v22 offset:1536
	ds_write_b32 v32, v23 offset:1792
	ds_write_b32 v32, v24 offset:2048
	ds_write_b32 v32, v25 offset:2304
	ds_write_b32 v32, v26 offset:2560
	ds_write_b32 v32, v27 offset:2816
	ds_write_b32 v32, v28 offset:3072
	ds_write_b32 v32, v29 offset:3328
	ds_write_b32 v32, v30 offset:3584
	ds_write_b32 v32, v31 offset:3840
	s_waitcnt lgkmcnt(0)
	s_barrier
	ds_read_b32 v16, v33 offset:0
	ds_read_b32 v17, v33 offset:4096
	ds_read_b32 v18, v33 offset:8192
	ds_read_b32 v19, v33 offset:12288
	ds_read_b32 v20, v33 offset:16384
	ds_read_b32 v21, v33 offset:20480
	ds_read_b32 v22, v33 offset:24576
	ds_read_b32 v23, v33 offset:28672
	ds_read_b32 v24, v33 offset:32768
	ds_read_b32 v25, v33 offset:36864
	ds_read_b32 v26, v33 offset:40960
	ds_read_b32 v27, v33 offset:45056
	ds_read_b32 v28, v33 offset:49152
	ds_read_b32 v29, v33 offset:53248
	ds_read_b32 v30, v33 offset:57344
	ds_read_b32 v31, v33 offset:61440
	s_waitcnt lgkmcnt(14)
	v_add_f32_e32 v16, v16, v17
	s_waitcnt lgkmcnt(13)
	v_add_f32_e32 v16, v16, v18
	s_waitcnt lgkmcnt(12)
	v_add_f32_e32 v16, v16, v19
	s_waitcnt lgkmcnt(11)
	v_add_f32_e32 v16, v16, v20
	s_waitcnt lgkmcnt(10)
	v_add_f32_e32 v16, v16, v21
	s_waitcnt lgkmcnt(9)
	v_add_f32_e32 v16, v16, v22
	s_waitcnt lgkmcnt(8)
	v_add_f32_e32 v16, v16, v23
	s_waitcnt lgkmcnt(7)
	v_add_f32_e32 v16, v16, v24
	s_waitcnt lgkmcnt(6)
	v_add_f32_e32 v16, v16, v25
	s_waitcnt lgkmcnt(5)
	v_add_f32_e32 v16, v16, v26
	s_waitcnt lgkmcnt(4)
	v_add_f32_e32 v16, v16, v27
	s_waitcnt lgkmcnt(3)
	v_add_f32_e32 v16, v16, v28
	s_waitcnt lgkmcnt(2)
	v_add_f32_e32 v16, v16, v29
	s_waitcnt lgkmcnt(1)
	v_add_f32_e32 v16, v16, v30
	s_waitcnt lgkmcnt(0)
	v_add_f32_e32 v16, v16, v31
	v_cvt_f16_f32_e32 v16, v16
	global_store_short v6, v16, s[16:17]
	s_endpgm

.LBB1_56:
	v_lshrrev_b32_e32 v1, 6, v0
	s_lshl_b32 s2, s2, 4
	s_mov_b32 s12, 0
	v_readfirstlane_b32 s3, v1
	s_nop 3
	s_mov_b32 s14, 0
	s_or_b32 s2, s2, s3
	s_cmpk_ge_i32 s2, 0xfb2
	s_cbranch_scc1 .LBB1_171
	s_mul_hi_u32 s8, s2, 0x63e7064
	s_mul_i32 s9, s8, 41
	s_sub_i32 s9, s2, s9
	s_lshl_b32 s10, s8, 6
	s_waitcnt lgkmcnt(0)
	s_add_u32 s10, s6, s10
	s_addc_u32 s11, s7, 0
	s_load_dwordx8 s[16:23], s[10:11], 0x0
	s_load_dword s24, s[10:11], 0x20
	v_mov_b32_e32 v6, s8
	v_mov_b32_e32 v39, 0
	s_waitcnt lgkmcnt(0)
	s_mov_b32 s15, s16
	s_add_i32 s13, s15, 31
	s_lshr_b32 s13, s13, 5
	s_cmp_lt_i32 s9, s13
	s_cbranch_scc1 .Lmy_send_found
	s_sub_i32 s9, s9, s13
	s_add_i32 s12, s12, s15
	s_add_i32 s14, s14, 1
	s_mov_b32 s15, s17
	s_add_i32 s13, s15, 31
	s_lshr_b32 s13, s13, 5
	s_cmp_lt_i32 s9, s13
	s_cbranch_scc1 .Lmy_send_found
	s_sub_i32 s9, s9, s13
	s_add_i32 s12, s12, s15
	s_add_i32 s14, s14, 1
	s_mov_b32 s15, s18
	s_add_i32 s13, s15, 31
	s_lshr_b32 s13, s13, 5
	s_cmp_lt_i32 s9, s13
	s_cbranch_scc1 .Lmy_send_found
	s_sub_i32 s9, s9, s13
	s_add_i32 s12, s12, s15
	s_add_i32 s14, s14, 1
	s_mov_b32 s15, s19
	s_add_i32 s13, s15, 31
	s_lshr_b32 s13, s13, 5
	s_cmp_lt_i32 s9, s13
	s_cbranch_scc1 .Lmy_send_found
	s_sub_i32 s9, s9, s13
	s_add_i32 s12, s12, s15
	s_add_i32 s14, s14, 1
	s_mov_b32 s15, s20
	s_add_i32 s13, s15, 31
	s_lshr_b32 s13, s13, 5
	s_cmp_lt_i32 s9, s13
	s_cbranch_scc1 .Lmy_send_found
	s_sub_i32 s9, s9, s13
	s_add_i32 s12, s12, s15
	s_add_i32 s14, s14, 1
	s_mov_b32 s15, s21
	s_add_i32 s13, s15, 31
	s_lshr_b32 s13, s13, 5
	s_cmp_lt_i32 s9, s13
	s_cbranch_scc1 .Lmy_send_found
	s_sub_i32 s9, s9, s13
	s_add_i32 s12, s12, s15
	s_add_i32 s14, s14, 1
	s_mov_b32 s15, s22
	s_add_i32 s13, s15, 31
	s_lshr_b32 s13, s13, 5
	s_cmp_lt_i32 s9, s13
	s_cbranch_scc1 .Lmy_send_found
	s_sub_i32 s9, s9, s13
	s_add_i32 s12, s12, s15
	s_add_i32 s14, s14, 1
	s_mov_b32 s15, s23
	s_add_i32 s13, s15, 31
	s_lshr_b32 s13, s13, 5
	s_cmp_lt_i32 s9, s13
	s_cbranch_scc1 .Lmy_send_found
	s_sub_i32 s9, s9, s13
	s_add_i32 s12, s12, s15
	s_add_i32 s14, s14, 1
	s_mov_b32 s15, s24
	s_add_i32 s13, s15, 31
	s_lshr_b32 s13, s13, 5
	s_cmp_lt_i32 s9, s13
	s_cbranch_scc1 .Lmy_send_found
	s_sub_i32 s9, s9, s13
	s_add_i32 s12, s12, s15
	s_add_i32 s14, s14, 1
	s_branch .LBB1_171

.LBB1_168:
	v_lshrrev_b32_e32 v9, 15, v5
	v_and_b32_e32 v9, 0x1fffc, v9
	v_add_u32_e32 v10, 0x22000, v9
	ds_add_rtn_u32 v10, v10, v4
	v_add_u32_e32 v9, 0x22800, v9
	ds_read_b32 v9, v9
	v_and_b32_e32 v5, 0x1ffff, v5
	s_waitcnt lgkmcnt(0)
	v_add_u32_e32 v10, v10, v9
	v_lshlrev_b32_e32 v10, 2, v10
	ds_write_b32 v10, v5
	s_or_b64 exec, exec, s[14:15]
	s_waitcnt vmcnt(0)
	v_cmp_lt_i32_e32 vcc, -1, v8
	s_and_saveexec_b64 s[14:15], vcc
	s_cbranch_execz .LBB1_139

.LBB1_170:
	s_or_b64 exec, exec, s[4:5]
	s_cbranch_execz .LBB1_56
	s_waitcnt lgkmcnt(0)
	s_barrier
	v_mov_b32_e32 v2, 0x227fc
	v_mov_b32_e32 v3, 0x22ffc
	ds_read_b32 v2, v2
	ds_read_b32 v3, v3
	v_lshlrev_b32_e32 v8, 2, v0
	v_add_u32_e32 v4, v6, v0
	v_ashrrev_i32_e32 v5, 31, v4
	v_lshl_add_u64 v[4:5], v[4:5], 2, s[12:13]
	v_mov_b32_e32 v9, v0
	s_mov_b64 s[24:25], 0x1000
	s_mov_b32 s21, 0
	s_waitcnt lgkmcnt(0)
	v_add_u32_e32 v2, v2, v3
	s_nop 0
	v_readfirstlane_b32 s20, v2
	s_nop 3
